# t16
# speedup vs baseline: 1.0167x; 1.0167x over previous
_Z11align_fusedPKfS0_PKiPf:
	s_load_dwordx8 s[4:11], s[0:1], 0x0
	s_mul_i32 s12, s2, 0x5dc0
	v_and_b32_e32 v7, 63, v0
	v_readfirstlane_b32 s13, v0
	v_lshlrev_b32_e32 v1, 4, v7
	v_mul_u32_u24_e32 v3, 12, v7
	s_mul_i32 s18, s13, 96
	s_mul_i32 s3, s13, 6
	s_sub_u32 s3, 0x49c, s3
	v_cmp_gt_u32_e64 s[14:15], s3, v7
	v_add_u32_e32 v2, s18, v1
	v_add_u32_e32 v3, s18, v3
	v_add_u32_e32 v4, 0x600, v3
	s_add_u32 s12, s12, s18
	s_add_u32 s12, s12, 0x800
	s_waitcnt lgkmcnt(0)
	s_add_u32 s4, s4, s12
	s_addc_u32 s5, s5, 0
	s_add_u32 s10, s10, s12
	s_addc_u32 s11, s11, 0
	s_cmp_lg_u32 s13, 0
	s_cbranch_scc1 .Lbulk_waves
	v_lshlrev_b32_e32 v5, 2, v7
	global_load_dword v5, v5, s[8:9]
	global_load_dwordx3 v[44:46], v3, s[6:7] nt
	global_load_dwordx4 v[8:11], v1, s[4:5] offset:-2048 nt
	global_load_dwordx4 v[12:15], v1, s[4:5] offset:-1024 nt
	global_load_dwordx4 v[16:19], v1, s[4:5] offset:0 nt
	global_load_dwordx4 v[20:23], v1, s[4:5] offset:1024 nt
	global_load_dwordx4 v[24:27], v1, s[4:5] offset:2048 nt
	global_load_dwordx4 v[28:31], v1, s[4:5] offset:3072 nt
	s_mov_b32 s20, 0
	s_mov_b32 s21, 0x10000
	s_mov_b32 s22, 0
	s_mov_b32 s23, 0x20000
	s_mov_b32 s24, 0
	s_mov_b32 s25, 0x40000
	s_mov_b32 s26, 0
	s_mov_b32 s27, 0x80000
	s_waitcnt vmcnt(6)
	v_mul_u32_u24_e32 v5, 12, v5
	v_add_f32_dpp v52, v44, v44 quad_perm:[1,0,3,2] row_mask:0xf bank_mask:0xf
	v_add_f32_dpp v53, v45, v45 quad_perm:[1,0,3,2] row_mask:0xf bank_mask:0xf
	v_add_f32_dpp v54, v46, v46 quad_perm:[1,0,3,2] row_mask:0xf bank_mask:0xf
	v_add_f32_dpp v52, v52, v52 quad_perm:[2,3,0,1] row_mask:0xf bank_mask:0xf
	v_add_f32_dpp v53, v53, v53 quad_perm:[2,3,0,1] row_mask:0xf bank_mask:0xf
	v_add_f32_dpp v54, v54, v54 quad_perm:[2,3,0,1] row_mask:0xf bank_mask:0xf
	v_add_f32_dpp v52, v52, v52 row_half_mirror row_mask:0xf bank_mask:0xf
	v_add_f32_dpp v53, v53, v53 row_half_mirror row_mask:0xf bank_mask:0xf
	v_add_f32_dpp v54, v54, v54 row_half_mirror row_mask:0xf bank_mask:0xf
	v_add_f32_dpp v52, v52, v52 row_mirror row_mask:0xf bank_mask:0xf
	v_add_f32_dpp v53, v53, v53 row_mirror row_mask:0xf bank_mask:0xf
	v_add_f32_dpp v54, v54, v54 row_mirror row_mask:0xf bank_mask:0xf
	v_add_f32_dpp v52, v52, v52 row_bcast:15 row_mask:0xa bank_mask:0xf
	v_add_f32_dpp v53, v53, v53 row_bcast:15 row_mask:0xa bank_mask:0xf
	v_add_f32_dpp v54, v54, v54 row_bcast:15 row_mask:0xa bank_mask:0xf
	v_add_f32_dpp v52, v52, v52 row_bcast:31 row_mask:0xc bank_mask:0xf
	v_add_f32_dpp v53, v53, v53 row_bcast:31 row_mask:0xc bank_mask:0xf
	v_add_f32_dpp v54, v54, v54 row_bcast:31 row_mask:0xc bank_mask:0xf
	v_readlane_b32 s28, v52, 63
	v_readlane_b32 s29, v53, 63
	v_readlane_b32 s30, v54, 63
	v_mov_b32_e32 v52, s28
	v_mov_b32_e32 v53, s29
	v_mov_b32_e32 v54, s30
	v_fmac_f32_e32 v44, 0xbc800000, v52
	v_fmac_f32_e32 v45, 0xbc800000, v53
	v_fmac_f32_e32 v46, 0xbc800000, v54
	s_waitcnt vmcnt(0)
	ds_write_b128 v2, v[8:11]
	ds_write_b128 v2, v[12:15] offset:1024
	ds_write_b128 v2, v[16:19] offset:2048
	ds_write_b128 v2, v[20:23] offset:3072
	ds_write_b128 v2, v[24:27] offset:4096
	ds_write_b128 v2, v[28:31] offset:5120
	s_waitcnt lgkmcnt(0)
	s_barrier
	ds_read_b32 v48, v5
	ds_read_b32 v49, v5 offset:4
	ds_read_b32 v50, v5 offset:8
	s_waitcnt lgkmcnt(0)
	v_add_f32_dpp v52, v48, v48 quad_perm:[1,0,3,2] row_mask:0xf bank_mask:0xf
	v_add_f32_dpp v53, v49, v49 quad_perm:[1,0,3,2] row_mask:0xf bank_mask:0xf
	v_add_f32_dpp v54, v50, v50 quad_perm:[1,0,3,2] row_mask:0xf bank_mask:0xf
	v_add_f32_dpp v52, v52, v52 quad_perm:[2,3,0,1] row_mask:0xf bank_mask:0xf
	v_add_f32_dpp v53, v53, v53 quad_perm:[2,3,0,1] row_mask:0xf bank_mask:0xf
	v_add_f32_dpp v54, v54, v54 quad_perm:[2,3,0,1] row_mask:0xf bank_mask:0xf
	v_add_f32_dpp v52, v52, v52 row_half_mirror row_mask:0xf bank_mask:0xf
	v_add_f32_dpp v53, v53, v53 row_half_mirror row_mask:0xf bank_mask:0xf
	v_add_f32_dpp v54, v54, v54 row_half_mirror row_mask:0xf bank_mask:0xf
	v_add_f32_dpp v52, v52, v52 row_mirror row_mask:0xf bank_mask:0xf
	v_add_f32_dpp v53, v53, v53 row_mirror row_mask:0xf bank_mask:0xf
	v_add_f32_dpp v54, v54, v54 row_mirror row_mask:0xf bank_mask:0xf
	v_add_f32_dpp v52, v52, v52 row_bcast:15 row_mask:0xa bank_mask:0xf
	v_add_f32_dpp v53, v53, v53 row_bcast:15 row_mask:0xa bank_mask:0xf
	v_add_f32_dpp v54, v54, v54 row_bcast:15 row_mask:0xa bank_mask:0xf
	v_add_f32_dpp v52, v52, v52 row_bcast:31 row_mask:0xc bank_mask:0xf
	v_add_f32_dpp v53, v53, v53 row_bcast:31 row_mask:0xc bank_mask:0xf
	v_add_f32_dpp v54, v54, v54 row_bcast:31 row_mask:0xc bank_mask:0xf
	v_readlane_b32 s32, v52, 63
	v_readlane_b32 s33, v53, 63
	v_readlane_b32 s34, v54, 63
	v_mov_b32_e32 v52, s32
	v_mov_b32_e32 v53, s33
	v_mov_b32_e32 v54, s34
	v_fmac_f32_e32 v48, 0xbc800000, v52
	v_fmac_f32_e32 v49, 0xbc800000, v53
	v_fmac_f32_e32 v50, 0xbc800000, v54
	v_mul_f32_e32 v52, v48, v44
	v_mul_f32_e32 v53, v48, v45
	v_mul_f32_e32 v54, v48, v46
	v_mul_f32_e32 v55, v49, v44
	v_mul_f32_e32 v56, v49, v45
	v_mul_f32_e32 v57, v49, v46
	v_mul_f32_e32 v58, v50, v44
	v_mul_f32_e32 v59, v50, v45
	v_mul_f32_e32 v60, v50, v46
	v_add_f32_dpp v52, v52, v52 quad_perm:[1,0,3,2] row_mask:0xf bank_mask:0xf
	v_add_f32_dpp v53, v53, v53 quad_perm:[1,0,3,2] row_mask:0xf bank_mask:0xf
	v_add_f32_dpp v54, v54, v54 quad_perm:[1,0,3,2] row_mask:0xf bank_mask:0xf
	v_add_f32_dpp v55, v55, v55 quad_perm:[1,0,3,2] row_mask:0xf bank_mask:0xf
	v_add_f32_dpp v56, v56, v56 quad_perm:[1,0,3,2] row_mask:0xf bank_mask:0xf
	v_add_f32_dpp v57, v57, v57 quad_perm:[1,0,3,2] row_mask:0xf bank_mask:0xf
	v_add_f32_dpp v58, v58, v58 quad_perm:[1,0,3,2] row_mask:0xf bank_mask:0xf
	v_add_f32_dpp v59, v59, v59 quad_perm:[1,0,3,2] row_mask:0xf bank_mask:0xf
	v_add_f32_dpp v60, v60, v60 quad_perm:[1,0,3,2] row_mask:0xf bank_mask:0xf
	v_add_f32_dpp v52, v52, v52 quad_perm:[2,3,0,1] row_mask:0xf bank_mask:0xf
	v_add_f32_dpp v53, v53, v53 quad_perm:[2,3,0,1] row_mask:0xf bank_mask:0xf
	v_add_f32_dpp v54, v54, v54 quad_perm:[2,3,0,1] row_mask:0xf bank_mask:0xf
	v_add_f32_dpp v55, v55, v55 quad_perm:[2,3,0,1] row_mask:0xf bank_mask:0xf
	v_add_f32_dpp v56, v56, v56 quad_perm:[2,3,0,1] row_mask:0xf bank_mask:0xf
	v_add_f32_dpp v57, v57, v57 quad_perm:[2,3,0,1] row_mask:0xf bank_mask:0xf
	v_add_f32_dpp v58, v58, v58 quad_perm:[2,3,0,1] row_mask:0xf bank_mask:0xf
	v_add_f32_dpp v59, v59, v59 quad_perm:[2,3,0,1] row_mask:0xf bank_mask:0xf
	v_add_f32_dpp v60, v60, v60 quad_perm:[2,3,0,1] row_mask:0xf bank_mask:0xf
	v_add_f32_dpp v52, v52, v52 row_half_mirror row_mask:0xf bank_mask:0xf
	v_add_f32_dpp v53, v53, v53 row_half_mirror row_mask:0xf bank_mask:0xf
	v_add_f32_dpp v54, v54, v54 row_half_mirror row_mask:0xf bank_mask:0xf
	v_add_f32_dpp v55, v55, v55 row_half_mirror row_mask:0xf bank_mask:0xf
	v_add_f32_dpp v56, v56, v56 row_half_mirror row_mask:0xf bank_mask:0xf
	v_add_f32_dpp v57, v57, v57 row_half_mirror row_mask:0xf bank_mask:0xf
	v_add_f32_dpp v58, v58, v58 row_half_mirror row_mask:0xf bank_mask:0xf
	v_add_f32_dpp v59, v59, v59 row_half_mirror row_mask:0xf bank_mask:0xf
	v_add_f32_dpp v60, v60, v60 row_half_mirror row_mask:0xf bank_mask:0xf
	v_add_f32_dpp v52, v52, v52 row_mirror row_mask:0xf bank_mask:0xf
	v_add_f32_dpp v53, v53, v53 row_mirror row_mask:0xf bank_mask:0xf
	v_add_f32_dpp v54, v54, v54 row_mirror row_mask:0xf bank_mask:0xf
	v_add_f32_dpp v55, v55, v55 row_mirror row_mask:0xf bank_mask:0xf
	v_add_f32_dpp v56, v56, v56 row_mirror row_mask:0xf bank_mask:0xf
	v_add_f32_dpp v57, v57, v57 row_mirror row_mask:0xf bank_mask:0xf
	v_add_f32_dpp v58, v58, v58 row_mirror row_mask:0xf bank_mask:0xf
	v_add_f32_dpp v59, v59, v59 row_mirror row_mask:0xf bank_mask:0xf
	v_add_f32_dpp v60, v60, v60 row_mirror row_mask:0xf bank_mask:0xf
	v_add_f32_dpp v52, v52, v52 row_bcast:15 row_mask:0xa bank_mask:0xf
	v_add_f32_dpp v53, v53, v53 row_bcast:15 row_mask:0xa bank_mask:0xf
	v_add_f32_dpp v54, v54, v54 row_bcast:15 row_mask:0xa bank_mask:0xf
	v_add_f32_dpp v55, v55, v55 row_bcast:15 row_mask:0xa bank_mask:0xf
	v_add_f32_dpp v56, v56, v56 row_bcast:15 row_mask:0xa bank_mask:0xf
	v_add_f32_dpp v57, v57, v57 row_bcast:15 row_mask:0xa bank_mask:0xf
	v_add_f32_dpp v58, v58, v58 row_bcast:15 row_mask:0xa bank_mask:0xf
	v_add_f32_dpp v59, v59, v59 row_bcast:15 row_mask:0xa bank_mask:0xf
	v_add_f32_dpp v60, v60, v60 row_bcast:15 row_mask:0xa bank_mask:0xf
	v_add_f32_dpp v52, v52, v52 row_bcast:31 row_mask:0xc bank_mask:0xf
	v_add_f32_dpp v53, v53, v53 row_bcast:31 row_mask:0xc bank_mask:0xf
	v_add_f32_dpp v54, v54, v54 row_bcast:31 row_mask:0xc bank_mask:0xf
	v_add_f32_dpp v55, v55, v55 row_bcast:31 row_mask:0xc bank_mask:0xf
	v_add_f32_dpp v56, v56, v56 row_bcast:31 row_mask:0xc bank_mask:0xf
	v_add_f32_dpp v57, v57, v57 row_bcast:31 row_mask:0xc bank_mask:0xf
	v_add_f32_dpp v58, v58, v58 row_bcast:31 row_mask:0xc bank_mask:0xf
	v_add_f32_dpp v59, v59, v59 row_bcast:31 row_mask:0xc bank_mask:0xf
	v_add_f32_dpp v60, v60, v60 row_bcast:31 row_mask:0xc bank_mask:0xf
	v_cndmask_b32_e64 v52, v52, v55, s[22:23]
	v_cndmask_b32_e64 v53, v53, v56, s[22:23]
	v_cndmask_b32_e64 v54, v54, v57, s[22:23]
	v_cndmask_b32_e64 v52, v52, v58, s[24:25]
	v_cndmask_b32_e64 v53, v53, v59, s[24:25]
	v_cndmask_b32_e64 v54, v54, v60, s[24:25]
	v_cndmask_b32_e64 v52, v52, 0, s[26:27]
	v_cndmask_b32_e64 v53, v53, 0, s[26:27]
	v_cndmask_b32_e64 v54, v54, 0, s[26:27]
	v_cndmask_b32_e64 v40, 0, 1.0, s[20:21]
	v_cndmask_b32_e64 v41, 0, 1.0, s[22:23]
	v_cndmask_b32_e64 v42, 0, 1.0, s[24:25]
	v_mul_f32_e32 v55, v52, v52
	v_mul_f32_e32 v56, v53, v53
	v_mul_f32_e32 v57, v52, v53
	v_add_f32_dpp v55, v55, v55 quad_perm:[1,0,3,2] row_mask:0xf bank_mask:0xf
	v_add_f32_dpp v56, v56, v56 quad_perm:[1,0,3,2] row_mask:0xf bank_mask:0xf
	v_add_f32_dpp v57, v57, v57 quad_perm:[1,0,3,2] row_mask:0xf bank_mask:0xf
	v_add_f32_dpp v55, v55, v55 quad_perm:[2,3,0,1] row_mask:0xf bank_mask:0xf
	v_add_f32_dpp v56, v56, v56 quad_perm:[2,3,0,1] row_mask:0xf bank_mask:0xf
	v_add_f32_dpp v57, v57, v57 quad_perm:[2,3,0,1] row_mask:0xf bank_mask:0xf
	v_sub_f32_e32 v60, v56, v55
	v_mul_f32_e32 v58, v57, v57
	v_cmp_gt_f32_e32 vcc, 0, v60
	v_mul_f32_e32 v59, v60, v60
	v_fmac_f32_e32 v59, 4.0, v58
	v_sqrt_f32_e32 v59, v59
	s_nop 0
	v_add_f32_e64 v59, |v60|, v59
	v_add_f32_e32 v59, 0x0da24260, v59
	v_rcp_f32_e32 v59, v59
	v_add_f32_e32 v58, v57, v57
	v_mul_f32_e32 v59, v58, v59
	v_cndmask_b32_e64 v59, v59, -v59, vcc
	v_fma_f32 v58, v59, v59, 1.0
	v_rsq_f32_e32 v61, v58
	s_nop 0
	v_mul_f32_e32 v62, v61, v59
	v_mul_f32_e32 v55, v62, v53
	v_mul_f32_e32 v56, v62, v52
	v_fma_f32 v52, v61, v52, -v55
	v_fma_f32 v53, v61, v53, v56
	v_mul_f32_e32 v55, v52, v52
	v_mul_f32_e32 v56, v54, v54
	v_mul_f32_e32 v57, v52, v54
	v_add_f32_dpp v55, v55, v55 quad_perm:[1,0,3,2] row_mask:0xf bank_mask:0xf
	v_add_f32_dpp v56, v56, v56 quad_perm:[1,0,3,2] row_mask:0xf bank_mask:0xf
	v_add_f32_dpp v57, v57, v57 quad_perm:[1,0,3,2] row_mask:0xf bank_mask:0xf
	v_add_f32_dpp v55, v55, v55 quad_perm:[2,3,0,1] row_mask:0xf bank_mask:0xf
	v_add_f32_dpp v56, v56, v56 quad_perm:[2,3,0,1] row_mask:0xf bank_mask:0xf
	v_add_f32_dpp v57, v57, v57 quad_perm:[2,3,0,1] row_mask:0xf bank_mask:0xf
	v_sub_f32_e32 v60, v56, v55
	v_mul_f32_e32 v58, v57, v57
	v_cmp_gt_f32_e32 vcc, 0, v60
	v_mul_f32_e32 v59, v60, v60
	v_fmac_f32_e32 v59, 4.0, v58
	v_sqrt_f32_e32 v59, v59
	v_mul_f32_e32 v63, v62, v41
	v_mul_f32_e32 v43, v62, v40
	v_fma_f32 v40, v61, v40, -v63
	v_fma_f32 v41, v61, v41, v43
	v_add_f32_e64 v59, |v60|, v59
	v_add_f32_e32 v59, 0x0da24260, v59
	v_rcp_f32_e32 v59, v59
	v_add_f32_e32 v58, v57, v57
	v_mul_f32_e32 v59, v58, v59
	v_cndmask_b32_e64 v59, v59, -v59, vcc
	v_fma_f32 v58, v59, v59, 1.0
	v_rsq_f32_e32 v61, v58
	s_nop 0
	v_mul_f32_e32 v62, v61, v59
	v_mul_f32_e32 v55, v62, v54
	v_mul_f32_e32 v56, v62, v52
	v_fma_f32 v52, v61, v52, -v55
	v_fma_f32 v54, v61, v54, v56
	v_mul_f32_e32 v55, v53, v53
	v_mul_f32_e32 v56, v54, v54
	v_mul_f32_e32 v57, v53, v54
	v_add_f32_dpp v55, v55, v55 quad_perm:[1,0,3,2] row_mask:0xf bank_mask:0xf
	v_add_f32_dpp v56, v56, v56 quad_perm:[1,0,3,2] row_mask:0xf bank_mask:0xf
	v_add_f32_dpp v57, v57, v57 quad_perm:[1,0,3,2] row_mask:0xf bank_mask:0xf
	v_add_f32_dpp v55, v55, v55 quad_perm:[2,3,0,1] row_mask:0xf bank_mask:0xf
	v_add_f32_dpp v56, v56, v56 quad_perm:[2,3,0,1] row_mask:0xf bank_mask:0xf
	v_add_f32_dpp v57, v57, v57 quad_perm:[2,3,0,1] row_mask:0xf bank_mask:0xf
	v_sub_f32_e32 v60, v56, v55
	v_mul_f32_e32 v58, v57, v57
	v_cmp_gt_f32_e32 vcc, 0, v60
	v_mul_f32_e32 v59, v60, v60
	v_fmac_f32_e32 v59, 4.0, v58
	v_sqrt_f32_e32 v59, v59
	v_mul_f32_e32 v63, v62, v42
	v_mul_f32_e32 v43, v62, v40
	v_fma_f32 v40, v61, v40, -v63
	v_fma_f32 v42, v61, v42, v43
	v_add_f32_e64 v59, |v60|, v59
	v_add_f32_e32 v59, 0x0da24260, v59
	v_rcp_f32_e32 v59, v59
	v_add_f32_e32 v58, v57, v57
	v_mul_f32_e32 v59, v58, v59
	v_cndmask_b32_e64 v59, v59, -v59, vcc
	v_fma_f32 v58, v59, v59, 1.0
	v_rsq_f32_e32 v61, v58
	s_nop 0
	v_mul_f32_e32 v62, v61, v59
	v_mul_f32_e32 v55, v62, v54
	v_mul_f32_e32 v56, v62, v53
	v_fma_f32 v53, v61, v53, -v55
	v_fma_f32 v54, v61, v54, v56
	v_mul_f32_e32 v55, v52, v52
	v_mul_f32_e32 v56, v53, v53
	v_mul_f32_e32 v57, v52, v53
	v_add_f32_dpp v55, v55, v55 quad_perm:[1,0,3,2] row_mask:0xf bank_mask:0xf
	v_add_f32_dpp v56, v56, v56 quad_perm:[1,0,3,2] row_mask:0xf bank_mask:0xf
	v_add_f32_dpp v57, v57, v57 quad_perm:[1,0,3,2] row_mask:0xf bank_mask:0xf
	v_add_f32_dpp v55, v55, v55 quad_perm:[2,3,0,1] row_mask:0xf bank_mask:0xf
	v_add_f32_dpp v56, v56, v56 quad_perm:[2,3,0,1] row_mask:0xf bank_mask:0xf
	v_add_f32_dpp v57, v57, v57 quad_perm:[2,3,0,1] row_mask:0xf bank_mask:0xf
	v_sub_f32_e32 v60, v56, v55
	v_mul_f32_e32 v58, v57, v57
	v_cmp_gt_f32_e32 vcc, 0, v60
	v_mul_f32_e32 v59, v60, v60
	v_fmac_f32_e32 v59, 4.0, v58
	v_sqrt_f32_e32 v59, v59
	v_mul_f32_e32 v63, v62, v42
	v_mul_f32_e32 v43, v62, v41
	v_fma_f32 v41, v61, v41, -v63
	v_fma_f32 v42, v61, v42, v43
	v_add_f32_e64 v59, |v60|, v59
	v_add_f32_e32 v59, 0x0da24260, v59
	v_rcp_f32_e32 v59, v59
	v_add_f32_e32 v58, v57, v57
	v_mul_f32_e32 v59, v58, v59
	v_cndmask_b32_e64 v59, v59, -v59, vcc
	v_fma_f32 v58, v59, v59, 1.0
	v_rsq_f32_e32 v61, v58
	s_nop 0
	v_mul_f32_e32 v62, v61, v59
	v_mul_f32_e32 v55, v62, v53
	v_mul_f32_e32 v56, v62, v52
	v_fma_f32 v52, v61, v52, -v55
	v_fma_f32 v53, v61, v53, v56
	v_mul_f32_e32 v55, v52, v52
	v_mul_f32_e32 v56, v54, v54
	v_mul_f32_e32 v57, v52, v54
	v_add_f32_dpp v55, v55, v55 quad_perm:[1,0,3,2] row_mask:0xf bank_mask:0xf
	v_add_f32_dpp v56, v56, v56 quad_perm:[1,0,3,2] row_mask:0xf bank_mask:0xf
	v_add_f32_dpp v57, v57, v57 quad_perm:[1,0,3,2] row_mask:0xf bank_mask:0xf
	v_add_f32_dpp v55, v55, v55 quad_perm:[2,3,0,1] row_mask:0xf bank_mask:0xf
	v_add_f32_dpp v56, v56, v56 quad_perm:[2,3,0,1] row_mask:0xf bank_mask:0xf
	v_add_f32_dpp v57, v57, v57 quad_perm:[2,3,0,1] row_mask:0xf bank_mask:0xf
	v_sub_f32_e32 v60, v56, v55
	v_mul_f32_e32 v58, v57, v57
	v_cmp_gt_f32_e32 vcc, 0, v60
	v_mul_f32_e32 v59, v60, v60
	v_fmac_f32_e32 v59, 4.0, v58
	v_sqrt_f32_e32 v59, v59
	v_mul_f32_e32 v63, v62, v41
	v_mul_f32_e32 v43, v62, v40
	v_fma_f32 v40, v61, v40, -v63
	v_fma_f32 v41, v61, v41, v43
	v_add_f32_e64 v59, |v60|, v59
	v_add_f32_e32 v59, 0x0da24260, v59
	v_rcp_f32_e32 v59, v59
	v_add_f32_e32 v58, v57, v57
	v_mul_f32_e32 v59, v58, v59
	v_cndmask_b32_e64 v59, v59, -v59, vcc
	v_fma_f32 v58, v59, v59, 1.0
	v_rsq_f32_e32 v61, v58
	s_nop 0
	v_mul_f32_e32 v62, v61, v59
	v_mul_f32_e32 v55, v62, v54
	v_mul_f32_e32 v56, v62, v52
	v_fma_f32 v52, v61, v52, -v55
	v_fma_f32 v54, v61, v54, v56
	v_mul_f32_e32 v55, v53, v53
	v_mul_f32_e32 v56, v54, v54
	v_mul_f32_e32 v57, v53, v54
	v_add_f32_dpp v55, v55, v55 quad_perm:[1,0,3,2] row_mask:0xf bank_mask:0xf
	v_add_f32_dpp v56, v56, v56 quad_perm:[1,0,3,2] row_mask:0xf bank_mask:0xf
	v_add_f32_dpp v57, v57, v57 quad_perm:[1,0,3,2] row_mask:0xf bank_mask:0xf
	v_add_f32_dpp v55, v55, v55 quad_perm:[2,3,0,1] row_mask:0xf bank_mask:0xf
	v_add_f32_dpp v56, v56, v56 quad_perm:[2,3,0,1] row_mask:0xf bank_mask:0xf
	v_add_f32_dpp v57, v57, v57 quad_perm:[2,3,0,1] row_mask:0xf bank_mask:0xf
	v_sub_f32_e32 v60, v56, v55
	v_mul_f32_e32 v58, v57, v57
	v_cmp_gt_f32_e32 vcc, 0, v60
	v_mul_f32_e32 v59, v60, v60
	v_fmac_f32_e32 v59, 4.0, v58
	v_sqrt_f32_e32 v59, v59
	v_mul_f32_e32 v63, v62, v42
	v_mul_f32_e32 v43, v62, v40
	v_fma_f32 v40, v61, v40, -v63
	v_fma_f32 v42, v61, v42, v43
	v_add_f32_e64 v59, |v60|, v59
	v_add_f32_e32 v59, 0x0da24260, v59
	v_rcp_f32_e32 v59, v59
	v_add_f32_e32 v58, v57, v57
	v_mul_f32_e32 v59, v58, v59
	v_cndmask_b32_e64 v59, v59, -v59, vcc
	v_fma_f32 v58, v59, v59, 1.0
	v_rsq_f32_e32 v61, v58
	s_nop 0
	v_mul_f32_e32 v62, v61, v59
	v_mul_f32_e32 v55, v62, v54
	v_mul_f32_e32 v56, v62, v53
	v_fma_f32 v53, v61, v53, -v55
	v_fma_f32 v54, v61, v54, v56
	v_mul_f32_e32 v55, v52, v52
	v_mul_f32_e32 v56, v53, v53
	v_mul_f32_e32 v57, v52, v53
	v_add_f32_dpp v55, v55, v55 quad_perm:[1,0,3,2] row_mask:0xf bank_mask:0xf
	v_add_f32_dpp v56, v56, v56 quad_perm:[1,0,3,2] row_mask:0xf bank_mask:0xf
	v_add_f32_dpp v57, v57, v57 quad_perm:[1,0,3,2] row_mask:0xf bank_mask:0xf
	v_add_f32_dpp v55, v55, v55 quad_perm:[2,3,0,1] row_mask:0xf bank_mask:0xf
	v_add_f32_dpp v56, v56, v56 quad_perm:[2,3,0,1] row_mask:0xf bank_mask:0xf
	v_add_f32_dpp v57, v57, v57 quad_perm:[2,3,0,1] row_mask:0xf bank_mask:0xf
	v_sub_f32_e32 v60, v56, v55
	v_mul_f32_e32 v58, v57, v57
	v_cmp_gt_f32_e32 vcc, 0, v60
	v_mul_f32_e32 v59, v60, v60
	v_fmac_f32_e32 v59, 4.0, v58
	v_sqrt_f32_e32 v59, v59
	v_mul_f32_e32 v63, v62, v42
	v_mul_f32_e32 v43, v62, v41
	v_fma_f32 v41, v61, v41, -v63
	v_fma_f32 v42, v61, v42, v43
	v_add_f32_e64 v59, |v60|, v59
	v_add_f32_e32 v59, 0x0da24260, v59
	v_rcp_f32_e32 v59, v59
	v_add_f32_e32 v58, v57, v57
	v_mul_f32_e32 v59, v58, v59
	v_cndmask_b32_e64 v59, v59, -v59, vcc
	v_fma_f32 v58, v59, v59, 1.0
	v_rsq_f32_e32 v61, v58
	s_nop 0
	v_mul_f32_e32 v62, v61, v59
	v_mul_f32_e32 v55, v62, v53
	v_mul_f32_e32 v56, v62, v52
	v_fma_f32 v52, v61, v52, -v55
	v_fma_f32 v53, v61, v53, v56
	v_mul_f32_e32 v55, v52, v52
	v_mul_f32_e32 v56, v54, v54
	v_mul_f32_e32 v57, v52, v54
	v_add_f32_dpp v55, v55, v55 quad_perm:[1,0,3,2] row_mask:0xf bank_mask:0xf
	v_add_f32_dpp v56, v56, v56 quad_perm:[1,0,3,2] row_mask:0xf bank_mask:0xf
	v_add_f32_dpp v57, v57, v57 quad_perm:[1,0,3,2] row_mask:0xf bank_mask:0xf
	v_add_f32_dpp v55, v55, v55 quad_perm:[2,3,0,1] row_mask:0xf bank_mask:0xf
	v_add_f32_dpp v56, v56, v56 quad_perm:[2,3,0,1] row_mask:0xf bank_mask:0xf
	v_add_f32_dpp v57, v57, v57 quad_perm:[2,3,0,1] row_mask:0xf bank_mask:0xf
	v_sub_f32_e32 v60, v56, v55
	v_mul_f32_e32 v58, v57, v57
	v_cmp_gt_f32_e32 vcc, 0, v60
	v_mul_f32_e32 v59, v60, v60
	v_fmac_f32_e32 v59, 4.0, v58
	v_sqrt_f32_e32 v59, v59
	v_mul_f32_e32 v63, v62, v41
	v_mul_f32_e32 v43, v62, v40
	v_fma_f32 v40, v61, v40, -v63
	v_fma_f32 v41, v61, v41, v43
	v_add_f32_e64 v59, |v60|, v59
	v_add_f32_e32 v59, 0x0da24260, v59
	v_rcp_f32_e32 v59, v59
	v_add_f32_e32 v58, v57, v57
	v_mul_f32_e32 v59, v58, v59
	v_cndmask_b32_e64 v59, v59, -v59, vcc
	v_fma_f32 v58, v59, v59, 1.0
	v_rsq_f32_e32 v61, v58
	s_nop 0
	v_mul_f32_e32 v62, v61, v59
	v_mul_f32_e32 v55, v62, v54
	v_mul_f32_e32 v56, v62, v52
	v_fma_f32 v52, v61, v52, -v55
	v_fma_f32 v54, v61, v54, v56
	v_mul_f32_e32 v55, v53, v53
	v_mul_f32_e32 v56, v54, v54
	v_mul_f32_e32 v57, v53, v54
	v_add_f32_dpp v55, v55, v55 quad_perm:[1,0,3,2] row_mask:0xf bank_mask:0xf
	v_add_f32_dpp v56, v56, v56 quad_perm:[1,0,3,2] row_mask:0xf bank_mask:0xf
	v_add_f32_dpp v57, v57, v57 quad_perm:[1,0,3,2] row_mask:0xf bank_mask:0xf
	v_add_f32_dpp v55, v55, v55 quad_perm:[2,3,0,1] row_mask:0xf bank_mask:0xf
	v_add_f32_dpp v56, v56, v56 quad_perm:[2,3,0,1] row_mask:0xf bank_mask:0xf
	v_add_f32_dpp v57, v57, v57 quad_perm:[2,3,0,1] row_mask:0xf bank_mask:0xf
	v_sub_f32_e32 v60, v56, v55
	v_mul_f32_e32 v58, v57, v57
	v_cmp_gt_f32_e32 vcc, 0, v60
	v_mul_f32_e32 v59, v60, v60
	v_fmac_f32_e32 v59, 4.0, v58
	v_sqrt_f32_e32 v59, v59
	v_mul_f32_e32 v63, v62, v42
	v_mul_f32_e32 v43, v62, v40
	v_fma_f32 v40, v61, v40, -v63
	v_fma_f32 v42, v61, v42, v43
	v_add_f32_e64 v59, |v60|, v59
	v_add_f32_e32 v59, 0x0da24260, v59
	v_rcp_f32_e32 v59, v59
	v_add_f32_e32 v58, v57, v57
	v_mul_f32_e32 v59, v58, v59
	v_cndmask_b32_e64 v59, v59, -v59, vcc
	v_fma_f32 v58, v59, v59, 1.0
	v_rsq_f32_e32 v61, v58
	s_nop 0
	v_mul_f32_e32 v62, v61, v59
	v_mul_f32_e32 v55, v62, v54
	v_mul_f32_e32 v56, v62, v53
	v_fma_f32 v53, v61, v53, -v55
	v_fma_f32 v54, v61, v54, v56
	v_mul_f32_e32 v55, v52, v52
	v_mul_f32_e32 v56, v53, v53
	v_mul_f32_e32 v57, v52, v53
	v_add_f32_dpp v55, v55, v55 quad_perm:[1,0,3,2] row_mask:0xf bank_mask:0xf
	v_add_f32_dpp v56, v56, v56 quad_perm:[1,0,3,2] row_mask:0xf bank_mask:0xf
	v_add_f32_dpp v57, v57, v57 quad_perm:[1,0,3,2] row_mask:0xf bank_mask:0xf
	v_add_f32_dpp v55, v55, v55 quad_perm:[2,3,0,1] row_mask:0xf bank_mask:0xf
	v_add_f32_dpp v56, v56, v56 quad_perm:[2,3,0,1] row_mask:0xf bank_mask:0xf
	v_add_f32_dpp v57, v57, v57 quad_perm:[2,3,0,1] row_mask:0xf bank_mask:0xf
	v_sub_f32_e32 v60, v56, v55
	v_mul_f32_e32 v58, v57, v57
	v_cmp_gt_f32_e32 vcc, 0, v60
	v_mul_f32_e32 v59, v60, v60
	v_fmac_f32_e32 v59, 4.0, v58
	v_sqrt_f32_e32 v59, v59
	v_mul_f32_e32 v63, v62, v42
	v_mul_f32_e32 v43, v62, v41
	v_fma_f32 v41, v61, v41, -v63
	v_fma_f32 v42, v61, v42, v43
	v_add_f32_e64 v59, |v60|, v59
	v_add_f32_e32 v59, 0x0da24260, v59
	v_rcp_f32_e32 v59, v59
	v_add_f32_e32 v58, v57, v57
	v_mul_f32_e32 v59, v58, v59
	v_cndmask_b32_e64 v59, v59, -v59, vcc
	v_fma_f32 v58, v59, v59, 1.0
	v_rsq_f32_e32 v61, v58
	s_nop 0
	v_mul_f32_e32 v62, v61, v59
	v_mul_f32_e32 v55, v62, v53
	v_mul_f32_e32 v56, v62, v52
	v_fma_f32 v52, v61, v52, -v55
	v_fma_f32 v53, v61, v53, v56
	v_mul_f32_e32 v55, v52, v52
	v_mul_f32_e32 v56, v54, v54
	v_mul_f32_e32 v57, v52, v54
	v_add_f32_dpp v55, v55, v55 quad_perm:[1,0,3,2] row_mask:0xf bank_mask:0xf
	v_add_f32_dpp v56, v56, v56 quad_perm:[1,0,3,2] row_mask:0xf bank_mask:0xf
	v_add_f32_dpp v57, v57, v57 quad_perm:[1,0,3,2] row_mask:0xf bank_mask:0xf
	v_add_f32_dpp v55, v55, v55 quad_perm:[2,3,0,1] row_mask:0xf bank_mask:0xf
	v_add_f32_dpp v56, v56, v56 quad_perm:[2,3,0,1] row_mask:0xf bank_mask:0xf
	v_add_f32_dpp v57, v57, v57 quad_perm:[2,3,0,1] row_mask:0xf bank_mask:0xf
	v_sub_f32_e32 v60, v56, v55
	v_mul_f32_e32 v58, v57, v57
	v_cmp_gt_f32_e32 vcc, 0, v60
	v_mul_f32_e32 v59, v60, v60
	v_fmac_f32_e32 v59, 4.0, v58
	v_sqrt_f32_e32 v59, v59
	v_mul_f32_e32 v63, v62, v41
	v_mul_f32_e32 v43, v62, v40
	v_fma_f32 v40, v61, v40, -v63
	v_fma_f32 v41, v61, v41, v43
	v_add_f32_e64 v59, |v60|, v59
	v_add_f32_e32 v59, 0x0da24260, v59
	v_rcp_f32_e32 v59, v59
	v_add_f32_e32 v58, v57, v57
	v_mul_f32_e32 v59, v58, v59
	v_cndmask_b32_e64 v59, v59, -v59, vcc
	v_fma_f32 v58, v59, v59, 1.0
	v_rsq_f32_e32 v61, v58
	s_nop 0
	v_mul_f32_e32 v62, v61, v59
	v_mul_f32_e32 v55, v62, v54
	v_mul_f32_e32 v56, v62, v52
	v_fma_f32 v52, v61, v52, -v55
	v_fma_f32 v54, v61, v54, v56
	v_mul_f32_e32 v55, v53, v53
	v_mul_f32_e32 v56, v54, v54
	v_mul_f32_e32 v57, v53, v54
	v_add_f32_dpp v55, v55, v55 quad_perm:[1,0,3,2] row_mask:0xf bank_mask:0xf
	v_add_f32_dpp v56, v56, v56 quad_perm:[1,0,3,2] row_mask:0xf bank_mask:0xf
	v_add_f32_dpp v57, v57, v57 quad_perm:[1,0,3,2] row_mask:0xf bank_mask:0xf
	v_add_f32_dpp v55, v55, v55 quad_perm:[2,3,0,1] row_mask:0xf bank_mask:0xf
	v_add_f32_dpp v56, v56, v56 quad_perm:[2,3,0,1] row_mask:0xf bank_mask:0xf
	v_add_f32_dpp v57, v57, v57 quad_perm:[2,3,0,1] row_mask:0xf bank_mask:0xf
	v_sub_f32_e32 v60, v56, v55
	v_mul_f32_e32 v58, v57, v57
	v_cmp_gt_f32_e32 vcc, 0, v60
	v_mul_f32_e32 v59, v60, v60
	v_fmac_f32_e32 v59, 4.0, v58
	v_sqrt_f32_e32 v59, v59
	v_mul_f32_e32 v63, v62, v42
	v_mul_f32_e32 v43, v62, v40
	v_fma_f32 v40, v61, v40, -v63
	v_fma_f32 v42, v61, v42, v43
	v_add_f32_e64 v59, |v60|, v59
	v_add_f32_e32 v59, 0x0da24260, v59
	v_rcp_f32_e32 v59, v59
	v_add_f32_e32 v58, v57, v57
	v_mul_f32_e32 v59, v58, v59
	v_cndmask_b32_e64 v59, v59, -v59, vcc
	v_fma_f32 v58, v59, v59, 1.0
	v_rsq_f32_e32 v61, v58
	s_nop 0
	v_mul_f32_e32 v62, v61, v59
	v_mul_f32_e32 v55, v62, v54
	v_mul_f32_e32 v56, v62, v53
	v_fma_f32 v53, v61, v53, -v55
	v_fma_f32 v54, v61, v54, v56
	v_mul_f32_e32 v63, v62, v42
	v_mul_f32_e32 v43, v62, v41
	v_fma_f32 v41, v61, v41, -v63
	v_fma_f32 v42, v61, v42, v43
	v_mul_f32_e32 v55, v52, v52
	v_mul_f32_e32 v56, v53, v53
	v_mul_f32_e32 v57, v54, v54
	v_add_f32_dpp v55, v55, v55 quad_perm:[1,0,3,2] row_mask:0xf bank_mask:0xf
	v_add_f32_dpp v56, v56, v56 quad_perm:[1,0,3,2] row_mask:0xf bank_mask:0xf
	v_add_f32_dpp v57, v57, v57 quad_perm:[1,0,3,2] row_mask:0xf bank_mask:0xf
	v_add_f32_dpp v55, v55, v55 quad_perm:[2,3,0,1] row_mask:0xf bank_mask:0xf
	v_add_f32_dpp v56, v56, v56 quad_perm:[2,3,0,1] row_mask:0xf bank_mask:0xf
	v_add_f32_dpp v57, v57, v57 quad_perm:[2,3,0,1] row_mask:0xf bank_mask:0xf
	v_cmp_le_f32_e64 s[28:29], v55, v56
	v_cmp_le_f32_e64 s[30:31], v55, v57
	v_cmp_lt_f32_e32 vcc, v57, v56
	s_and_b64 s[28:29], s[28:29], s[30:31]
	s_andn2_b64 s[30:31], vcc, s[28:29]
	v_cndmask_b32_e64 v44, v52, v53, s[28:29]
	v_cndmask_b32_e64 v45, v54, v53, s[30:31]
	v_cndmask_b32_e64 v46, v40, v41, s[28:29]
	v_cndmask_b32_e64 v47, v42, v41, s[30:31]
	v_mul_f32_e32 v58, v44, v44
	s_nop 1
	v_add_f32_dpp v58, v58, v58 quad_perm:[1,0,3,2] row_mask:0xf bank_mask:0xf
	s_nop 1
	v_add_f32_dpp v58, v58, v58 quad_perm:[2,3,0,1] row_mask:0xf bank_mask:0xf
	v_max_f32_e32 v58, 0x3aa2425, v58
	v_rsq_f32_e32 v58, v58
	s_nop 0
	v_mul_f32_e32 v48, v44, v58
	v_mul_f32_e32 v59, v48, v45
	s_nop 1
	v_add_f32_dpp v59, v59, v59 quad_perm:[1,0,3,2] row_mask:0xf bank_mask:0xf
	s_nop 1
	v_add_f32_dpp v59, v59, v59 quad_perm:[2,3,0,1] row_mask:0xf bank_mask:0xf
	v_fma_f32 v49, -v59, v48, v45
	v_mul_f32_e32 v58, v49, v49
	s_nop 1
	v_add_f32_dpp v58, v58, v58 quad_perm:[1,0,3,2] row_mask:0xf bank_mask:0xf
	s_nop 1
	v_add_f32_dpp v58, v58, v58 quad_perm:[2,3,0,1] row_mask:0xf bank_mask:0xf
	v_max_f32_e32 v58, 0x3aa2425, v58
	v_rsq_f32_e32 v58, v58
	s_nop 0
	v_mul_f32_e32 v50, v49, v58
	v_mov_b32_dpp v43, v47 quad_perm:[2,0,1,3] row_mask:0xf bank_mask:0xf
	v_mov_b32_dpp v63, v47 quad_perm:[1,2,0,3] row_mask:0xf bank_mask:0xf
	v_mov_b32_dpp v62, v50 quad_perm:[2,0,1,3] row_mask:0xf bank_mask:0xf
	v_mov_b32_dpp v61, v50 quad_perm:[1,2,0,3] row_mask:0xf bank_mask:0xf
	v_mul_f32_dpp v60, v46, v43 quad_perm:[1,2,0,3] row_mask:0xf bank_mask:0xf
	v_mul_f32_dpp v51, v48, v62 quad_perm:[1,2,0,3] row_mask:0xf bank_mask:0xf
	s_nop 0
	v_fmac_f32_dpp v60, -v46, v63 quad_perm:[2,0,1,3] row_mask:0xf bank_mask:0xf
	v_fmac_f32_dpp v51, -v48, v61 quad_perm:[2,0,1,3] row_mask:0xf bank_mask:0xf
	v_mul_f32_dpp v52, v46, v48 quad_perm:[0,0,0,0] row_mask:0xf bank_mask:0xf
	v_mul_f32_dpp v53, v46, v48 quad_perm:[1,1,1,1] row_mask:0xf bank_mask:0xf
	v_mul_f32_dpp v54, v46, v48 quad_perm:[2,2,2,2] row_mask:0xf bank_mask:0xf
	v_fmac_f32_dpp v52, v47, v50 quad_perm:[0,0,0,0] row_mask:0xf bank_mask:0xf
	v_fmac_f32_dpp v53, v47, v50 quad_perm:[1,1,1,1] row_mask:0xf bank_mask:0xf
	v_fmac_f32_dpp v54, v47, v50 quad_perm:[2,2,2,2] row_mask:0xf bank_mask:0xf
	v_fmac_f32_dpp v52, v60, v51 quad_perm:[0,0,0,0] row_mask:0xf bank_mask:0xf
	v_fmac_f32_dpp v53, v60, v51 quad_perm:[1,1,1,1] row_mask:0xf bank_mask:0xf
	v_fmac_f32_dpp v54, v60, v51 quad_perm:[2,2,2,2] row_mask:0xf bank_mask:0xf
	v_mov_b32_e32 v55, 0
	v_writelane_b32 v55, s32, 48
	v_writelane_b32 v55, s33, 49
	v_writelane_b32 v55, s34, 50
	v_mul_f32_e32 v55, 0xbc800000, v55
	v_mul_f32_e32 v56, v55, v52
	v_mul_f32_e32 v57, v55, v53
	v_mul_f32_e32 v58, v55, v54
	v_add_f32_dpp v56, v56, v56 quad_perm:[1,0,3,2] row_mask:0xf bank_mask:0xf
	v_add_f32_dpp v57, v57, v57 quad_perm:[1,0,3,2] row_mask:0xf bank_mask:0xf
	v_add_f32_dpp v58, v58, v58 quad_perm:[1,0,3,2] row_mask:0xf bank_mask:0xf
	v_add_f32_dpp v56, v56, v56 quad_perm:[2,3,0,1] row_mask:0xf bank_mask:0xf
	v_add_f32_dpp v57, v57, v57 quad_perm:[2,3,0,1] row_mask:0xf bank_mask:0xf
	v_add_f32_dpp v58, v58, v58 quad_perm:[2,3,0,1] row_mask:0xf bank_mask:0xf
	v_cndmask_b32_e64 v52, v52, v56, s[26:27]
	v_cndmask_b32_e64 v53, v53, v57, s[26:27]
	v_cndmask_b32_e64 v54, v54, v58, s[26:27]
	v_subrev_u32_e32 v59, 48, v0
	v_lshlrev_b32_e32 v59, 4, v59
	s_mov_b32 s20, 0
	s_mov_b32 s21, 0xf0000
	s_mov_b64 exec, s[20:21]
	ds_write_b96 v59, v[52:54] offset:24576
	s_mov_b64 exec, -1
	s_waitcnt lgkmcnt(0)
	s_branch .Ljoin
